# lever 7 (instruction selection away from MFMAs): GDN step 4 forward substitution and block products with v_pk_fma_f32 / v_pk_mul_f32 (two f32 FMAs per instruction, f32 throughout); counted unit-head w
# baseline (speedup 1.0000x reference)
.LBB0_1574:
	s_or_b64 exec, exec, s[0:1]
	s_waitcnt lgkmcnt(0)
	s_barrier
	s_cmp_gt_u32 s10, 1
	s_cbranch_scc1 .Lg4_s1done
	v_lshrrev_b32_e32 v4, 5, v21
	v_and_b32_e32 v108, 31, v21
	s_mul_i32 s1, s10, 0x4800
	v_mul_u32_u24_e32 v5, 0x2280, v4
	s_mul_i32 s11, s10, 0x3000
	v_lshlrev_b32_e32 v6, 12, v4
	v_add3_u32 v109, v61, v5, s1
	s_add_i32 s11, s11, 0x1b000
	v_lshl_add_u32 v6, v108, 2, v6
	v_add3_u32 v1, v61, v6, s11
	v_cmp_eq_u32_e32 vcc, 0, v108
	ds_read_b128 v[168:171], v109 offset:272
	s_nop 0
	v_cndmask_b32_e64 v72, 0, 1.0, vcc
	v_cmp_eq_u32_e32 vcc, 1, v108
	ds_read_b128 v[136:139], v109 offset:544
	s_nop 0
	s_waitcnt lgkmcnt(1)
	v_cndmask_b32_e64 v110, 0, 1.0, vcc
	v_fma_f32 v110, -v168, v72, v110
	v_mov_b32_e32 v73, v110
	v_cmp_eq_u32_e32 vcc, 2, v108
	ds_read_b128 v[168:171], v109 offset:816
	s_nop 0
	s_waitcnt lgkmcnt(1)
	v_pk_mul_f32 v[104:105], v[136:137], v[72:73] neg_lo:[1,0] neg_hi:[1,0]
	v_cndmask_b32_e64 v110, 0, 1.0, vcc
	v_add_f32_e32 v104, v104, v105
	v_add_f32_e32 v74, v104, v110
	v_cmp_eq_u32_e32 vcc, 3, v108
	ds_read_b128 v[136:139], v109 offset:1088
	s_nop 0
	s_waitcnt lgkmcnt(1)
	v_pk_mul_f32 v[104:105], v[168:169], v[72:73] neg_lo:[1,0] neg_hi:[1,0]
	v_cndmask_b32_e64 v110, 0, 1.0, vcc
	v_fma_f32 v110, -v170, v74, v110
	v_add_f32_e32 v104, v104, v105
	v_add_f32_e32 v75, v104, v110
	v_cmp_eq_u32_e32 vcc, 4, v108
	ds_read_b128 v[168:171], v109 offset:1360
	ds_read_b128 v[172:175], v109 offset:1376
	s_waitcnt lgkmcnt(2)
	v_pk_mul_f32 v[104:105], v[136:137], v[72:73] neg_lo:[1,0] neg_hi:[1,0]
	v_pk_mul_f32 v[106:107], v[138:139], v[74:75] neg_lo:[1,0] neg_hi:[1,0]
	v_cndmask_b32_e64 v110, 0, 1.0, vcc
	v_pk_add_f32 v[104:105], v[104:105], v[106:107]
	v_add_f32_e32 v110, v110, v104
	v_add_f32_e32 v76, v110, v105
	v_cmp_eq_u32_e32 vcc, 5, v108
	ds_read_b128 v[136:139], v109 offset:1632
	ds_read_b128 v[140:143], v109 offset:1648
	s_waitcnt lgkmcnt(2)
	v_pk_mul_f32 v[104:105], v[168:169], v[72:73] neg_lo:[1,0] neg_hi:[1,0]
	v_pk_mul_f32 v[106:107], v[170:171], v[74:75] neg_lo:[1,0] neg_hi:[1,0]
	v_cndmask_b32_e64 v110, 0, 1.0, vcc
	v_fma_f32 v110, -v172, v76, v110
	v_pk_add_f32 v[104:105], v[104:105], v[106:107]
	v_add_f32_e32 v110, v110, v104
	v_add_f32_e32 v77, v110, v105
	v_cmp_eq_u32_e32 vcc, 6, v108
	ds_read_b128 v[168:171], v109 offset:1904
	ds_read_b128 v[172:175], v109 offset:1920
	s_waitcnt lgkmcnt(2)
	v_pk_mul_f32 v[104:105], v[136:137], v[72:73] neg_lo:[1,0] neg_hi:[1,0]
	v_pk_mul_f32 v[106:107], v[138:139], v[74:75] neg_lo:[1,0] neg_hi:[1,0]
	v_pk_fma_f32 v[104:105], v[140:141], v[76:77], v[104:105] neg_lo:[1,0,0] neg_hi:[1,0,0]
	v_cndmask_b32_e64 v110, 0, 1.0, vcc
	v_pk_add_f32 v[104:105], v[104:105], v[106:107]
	v_add_f32_e32 v110, v110, v104
	v_add_f32_e32 v78, v110, v105
	v_cmp_eq_u32_e32 vcc, 7, v108
	ds_read_b128 v[136:139], v109 offset:2176
	ds_read_b128 v[140:143], v109 offset:2192
	s_waitcnt lgkmcnt(2)
	v_pk_mul_f32 v[104:105], v[168:169], v[72:73] neg_lo:[1,0] neg_hi:[1,0]
	v_pk_mul_f32 v[106:107], v[170:171], v[74:75] neg_lo:[1,0] neg_hi:[1,0]
	v_pk_fma_f32 v[104:105], v[172:173], v[76:77], v[104:105] neg_lo:[1,0,0] neg_hi:[1,0,0]
	v_cndmask_b32_e64 v110, 0, 1.0, vcc
	v_fma_f32 v110, -v174, v78, v110
	v_pk_add_f32 v[104:105], v[104:105], v[106:107]
	v_add_f32_e32 v110, v110, v104
	v_add_f32_e32 v79, v110, v105
	v_cmp_eq_u32_e32 vcc, 8, v108
	ds_read_b128 v[168:171], v109 offset:2448
	ds_read_b128 v[172:175], v109 offset:2464
	ds_read_b128 v[176:179], v109 offset:2480
	s_waitcnt lgkmcnt(3)
	v_pk_mul_f32 v[104:105], v[136:137], v[72:73] neg_lo:[1,0] neg_hi:[1,0]
	v_pk_mul_f32 v[106:107], v[138:139], v[74:75] neg_lo:[1,0] neg_hi:[1,0]
	v_pk_fma_f32 v[104:105], v[140:141], v[76:77], v[104:105] neg_lo:[1,0,0] neg_hi:[1,0,0]
	v_pk_fma_f32 v[106:107], v[142:143], v[78:79], v[106:107] neg_lo:[1,0,0] neg_hi:[1,0,0]
	v_cndmask_b32_e64 v110, 0, 1.0, vcc
	v_pk_add_f32 v[104:105], v[104:105], v[106:107]
	v_add_f32_e32 v110, v110, v104
	v_add_f32_e32 v80, v110, v105
	v_cmp_eq_u32_e32 vcc, 9, v108
	ds_read_b128 v[136:139], v109 offset:2720
	ds_read_b128 v[140:143], v109 offset:2736
	ds_read_b128 v[144:147], v109 offset:2752
	s_waitcnt lgkmcnt(3)
	v_pk_mul_f32 v[104:105], v[168:169], v[72:73] neg_lo:[1,0] neg_hi:[1,0]
	v_pk_mul_f32 v[106:107], v[170:171], v[74:75] neg_lo:[1,0] neg_hi:[1,0]
	v_pk_fma_f32 v[104:105], v[172:173], v[76:77], v[104:105] neg_lo:[1,0,0] neg_hi:[1,0,0]
	v_pk_fma_f32 v[106:107], v[174:175], v[78:79], v[106:107] neg_lo:[1,0,0] neg_hi:[1,0,0]
	v_cndmask_b32_e64 v110, 0, 1.0, vcc
	v_fma_f32 v110, -v176, v80, v110
	v_pk_add_f32 v[104:105], v[104:105], v[106:107]
	v_add_f32_e32 v110, v110, v104
	v_add_f32_e32 v81, v110, v105
	v_cmp_eq_u32_e32 vcc, 10, v108
	ds_read_b128 v[168:171], v109 offset:2992
	ds_read_b128 v[172:175], v109 offset:3008
	ds_read_b128 v[176:179], v109 offset:3024
	s_waitcnt lgkmcnt(3)
	v_pk_mul_f32 v[104:105], v[136:137], v[72:73] neg_lo:[1,0] neg_hi:[1,0]
	v_pk_mul_f32 v[106:107], v[138:139], v[74:75] neg_lo:[1,0] neg_hi:[1,0]
	v_pk_fma_f32 v[104:105], v[140:141], v[76:77], v[104:105] neg_lo:[1,0,0] neg_hi:[1,0,0]
	v_pk_fma_f32 v[106:107], v[142:143], v[78:79], v[106:107] neg_lo:[1,0,0] neg_hi:[1,0,0]
	v_pk_fma_f32 v[104:105], v[144:145], v[80:81], v[104:105] neg_lo:[1,0,0] neg_hi:[1,0,0]
	v_cndmask_b32_e64 v110, 0, 1.0, vcc
	v_pk_add_f32 v[104:105], v[104:105], v[106:107]
	v_add_f32_e32 v110, v110, v104
	v_add_f32_e32 v82, v110, v105
	v_cmp_eq_u32_e32 vcc, 11, v108
	ds_read_b128 v[136:139], v109 offset:3264
	ds_read_b128 v[140:143], v109 offset:3280
	ds_read_b128 v[144:147], v109 offset:3296
	s_waitcnt lgkmcnt(3)
	v_pk_mul_f32 v[104:105], v[168:169], v[72:73] neg_lo:[1,0] neg_hi:[1,0]
	v_pk_mul_f32 v[106:107], v[170:171], v[74:75] neg_lo:[1,0] neg_hi:[1,0]
	v_pk_fma_f32 v[104:105], v[172:173], v[76:77], v[104:105] neg_lo:[1,0,0] neg_hi:[1,0,0]
	v_pk_fma_f32 v[106:107], v[174:175], v[78:79], v[106:107] neg_lo:[1,0,0] neg_hi:[1,0,0]
	v_pk_fma_f32 v[104:105], v[176:177], v[80:81], v[104:105] neg_lo:[1,0,0] neg_hi:[1,0,0]
	v_cndmask_b32_e64 v110, 0, 1.0, vcc
	v_fma_f32 v110, -v178, v82, v110
	v_pk_add_f32 v[104:105], v[104:105], v[106:107]
	v_add_f32_e32 v110, v110, v104
	v_add_f32_e32 v83, v110, v105
	v_cmp_eq_u32_e32 vcc, 12, v108
	ds_read_b128 v[168:171], v109 offset:3536
	ds_read_b128 v[172:175], v109 offset:3552
	ds_read_b128 v[176:179], v109 offset:3568
	ds_read_b128 v[180:183], v109 offset:3584
	s_waitcnt lgkmcnt(4)
	v_pk_mul_f32 v[104:105], v[136:137], v[72:73] neg_lo:[1,0] neg_hi:[1,0]
	v_pk_mul_f32 v[106:107], v[138:139], v[74:75] neg_lo:[1,0] neg_hi:[1,0]
	v_pk_fma_f32 v[104:105], v[140:141], v[76:77], v[104:105] neg_lo:[1,0,0] neg_hi:[1,0,0]
	v_pk_fma_f32 v[106:107], v[142:143], v[78:79], v[106:107] neg_lo:[1,0,0] neg_hi:[1,0,0]
	v_pk_fma_f32 v[104:105], v[144:145], v[80:81], v[104:105] neg_lo:[1,0,0] neg_hi:[1,0,0]
	v_pk_fma_f32 v[106:107], v[146:147], v[82:83], v[106:107] neg_lo:[1,0,0] neg_hi:[1,0,0]
	v_cndmask_b32_e64 v110, 0, 1.0, vcc
	v_pk_add_f32 v[104:105], v[104:105], v[106:107]
	v_add_f32_e32 v110, v110, v104
	v_add_f32_e32 v84, v110, v105
	v_cmp_eq_u32_e32 vcc, 13, v108
	ds_read_b128 v[136:139], v109 offset:3808
	ds_read_b128 v[140:143], v109 offset:3824
	ds_read_b128 v[144:147], v109 offset:3840
	ds_read_b128 v[148:151], v109 offset:3856
	s_waitcnt lgkmcnt(4)
	v_pk_mul_f32 v[104:105], v[168:169], v[72:73] neg_lo:[1,0] neg_hi:[1,0]
	v_pk_mul_f32 v[106:107], v[170:171], v[74:75] neg_lo:[1,0] neg_hi:[1,0]
	v_pk_fma_f32 v[104:105], v[172:173], v[76:77], v[104:105] neg_lo:[1,0,0] neg_hi:[1,0,0]
	v_pk_fma_f32 v[106:107], v[174:175], v[78:79], v[106:107] neg_lo:[1,0,0] neg_hi:[1,0,0]
	v_pk_fma_f32 v[104:105], v[176:177], v[80:81], v[104:105] neg_lo:[1,0,0] neg_hi:[1,0,0]
	v_pk_fma_f32 v[106:107], v[178:179], v[82:83], v[106:107] neg_lo:[1,0,0] neg_hi:[1,0,0]
	v_cndmask_b32_e64 v110, 0, 1.0, vcc
	v_fma_f32 v110, -v180, v84, v110
	v_pk_add_f32 v[104:105], v[104:105], v[106:107]
	v_add_f32_e32 v110, v110, v104
	v_add_f32_e32 v85, v110, v105
	v_cmp_eq_u32_e32 vcc, 14, v108
	ds_read_b128 v[168:171], v109 offset:4080
	ds_read_b128 v[172:175], v109 offset:4096
	ds_read_b128 v[176:179], v109 offset:4112
	ds_read_b128 v[180:183], v109 offset:4128
	s_waitcnt lgkmcnt(4)
	v_pk_mul_f32 v[104:105], v[136:137], v[72:73] neg_lo:[1,0] neg_hi:[1,0]
	v_pk_mul_f32 v[106:107], v[138:139], v[74:75] neg_lo:[1,0] neg_hi:[1,0]
	v_pk_fma_f32 v[104:105], v[140:141], v[76:77], v[104:105] neg_lo:[1,0,0] neg_hi:[1,0,0]
	v_pk_fma_f32 v[106:107], v[142:143], v[78:79], v[106:107] neg_lo:[1,0,0] neg_hi:[1,0,0]
	v_pk_fma_f32 v[104:105], v[144:145], v[80:81], v[104:105] neg_lo:[1,0,0] neg_hi:[1,0,0]
	v_pk_fma_f32 v[106:107], v[146:147], v[82:83], v[106:107] neg_lo:[1,0,0] neg_hi:[1,0,0]
	v_pk_fma_f32 v[104:105], v[148:149], v[84:85], v[104:105] neg_lo:[1,0,0] neg_hi:[1,0,0]
	v_cndmask_b32_e64 v110, 0, 1.0, vcc
	v_pk_add_f32 v[104:105], v[104:105], v[106:107]
	v_add_f32_e32 v110, v110, v104
	v_add_f32_e32 v86, v110, v105
	v_cmp_eq_u32_e32 vcc, 15, v108
	ds_read_b128 v[136:139], v109 offset:4352
	ds_read_b128 v[140:143], v109 offset:4368
	ds_read_b128 v[144:147], v109 offset:4384
	ds_read_b128 v[148:151], v109 offset:4400
	s_waitcnt lgkmcnt(4)
	v_pk_mul_f32 v[104:105], v[168:169], v[72:73] neg_lo:[1,0] neg_hi:[1,0]
	v_pk_mul_f32 v[106:107], v[170:171], v[74:75] neg_lo:[1,0] neg_hi:[1,0]
	v_pk_fma_f32 v[104:105], v[172:173], v[76:77], v[104:105] neg_lo:[1,0,0] neg_hi:[1,0,0]
	v_pk_fma_f32 v[106:107], v[174:175], v[78:79], v[106:107] neg_lo:[1,0,0] neg_hi:[1,0,0]
	v_pk_fma_f32 v[104:105], v[176:177], v[80:81], v[104:105] neg_lo:[1,0,0] neg_hi:[1,0,0]
	v_pk_fma_f32 v[106:107], v[178:179], v[82:83], v[106:107] neg_lo:[1,0,0] neg_hi:[1,0,0]
	v_pk_fma_f32 v[104:105], v[180:181], v[84:85], v[104:105] neg_lo:[1,0,0] neg_hi:[1,0,0]
	v_cndmask_b32_e64 v110, 0, 1.0, vcc
	v_fma_f32 v110, -v182, v86, v110
	v_pk_add_f32 v[104:105], v[104:105], v[106:107]
	v_add_f32_e32 v110, v110, v104
	v_add_f32_e32 v87, v110, v105
	v_cmp_eq_u32_e32 vcc, 16, v108
	ds_read_b128 v[168:171], v109 offset:4624
	ds_read_b128 v[172:175], v109 offset:4640
	ds_read_b128 v[176:179], v109 offset:4656
	ds_read_b128 v[180:183], v109 offset:4672
	ds_read_b128 v[184:187], v109 offset:4688
	s_waitcnt lgkmcnt(5)
	v_pk_mul_f32 v[104:105], v[136:137], v[72:73] neg_lo:[1,0] neg_hi:[1,0]
	v_pk_mul_f32 v[106:107], v[138:139], v[74:75] neg_lo:[1,0] neg_hi:[1,0]
	v_pk_fma_f32 v[104:105], v[140:141], v[76:77], v[104:105] neg_lo:[1,0,0] neg_hi:[1,0,0]
	v_pk_fma_f32 v[106:107], v[142:143], v[78:79], v[106:107] neg_lo:[1,0,0] neg_hi:[1,0,0]
	v_pk_fma_f32 v[104:105], v[144:145], v[80:81], v[104:105] neg_lo:[1,0,0] neg_hi:[1,0,0]
	v_pk_fma_f32 v[106:107], v[146:147], v[82:83], v[106:107] neg_lo:[1,0,0] neg_hi:[1,0,0]
	v_pk_fma_f32 v[104:105], v[148:149], v[84:85], v[104:105] neg_lo:[1,0,0] neg_hi:[1,0,0]
	v_pk_fma_f32 v[106:107], v[150:151], v[86:87], v[106:107] neg_lo:[1,0,0] neg_hi:[1,0,0]
	v_cndmask_b32_e64 v110, 0, 1.0, vcc
	v_pk_add_f32 v[104:105], v[104:105], v[106:107]
	v_add_f32_e32 v110, v110, v104
	v_add_f32_e32 v88, v110, v105
	v_cmp_eq_u32_e32 vcc, 17, v108
	ds_read_b128 v[136:139], v109 offset:4896
	ds_read_b128 v[140:143], v109 offset:4912
	ds_read_b128 v[144:147], v109 offset:4928
	ds_read_b128 v[148:151], v109 offset:4944
	ds_read_b128 v[152:155], v109 offset:4960
	s_waitcnt lgkmcnt(5)
	v_pk_mul_f32 v[104:105], v[168:169], v[72:73] neg_lo:[1,0] neg_hi:[1,0]
	v_pk_mul_f32 v[106:107], v[170:171], v[74:75] neg_lo:[1,0] neg_hi:[1,0]
	v_pk_fma_f32 v[104:105], v[172:173], v[76:77], v[104:105] neg_lo:[1,0,0] neg_hi:[1,0,0]
	v_pk_fma_f32 v[106:107], v[174:175], v[78:79], v[106:107] neg_lo:[1,0,0] neg_hi:[1,0,0]
	v_pk_fma_f32 v[104:105], v[176:177], v[80:81], v[104:105] neg_lo:[1,0,0] neg_hi:[1,0,0]
	v_pk_fma_f32 v[106:107], v[178:179], v[82:83], v[106:107] neg_lo:[1,0,0] neg_hi:[1,0,0]
	v_pk_fma_f32 v[104:105], v[180:181], v[84:85], v[104:105] neg_lo:[1,0,0] neg_hi:[1,0,0]
	v_pk_fma_f32 v[106:107], v[182:183], v[86:87], v[106:107] neg_lo:[1,0,0] neg_hi:[1,0,0]
	v_cndmask_b32_e64 v110, 0, 1.0, vcc
	v_fma_f32 v110, -v184, v88, v110
	v_pk_add_f32 v[104:105], v[104:105], v[106:107]
	v_add_f32_e32 v110, v110, v104
	v_add_f32_e32 v89, v110, v105
	v_cmp_eq_u32_e32 vcc, 18, v108
	ds_read_b128 v[168:171], v109 offset:5168
	ds_read_b128 v[172:175], v109 offset:5184
	ds_read_b128 v[176:179], v109 offset:5200
	ds_read_b128 v[180:183], v109 offset:5216
	ds_read_b128 v[184:187], v109 offset:5232
	s_waitcnt lgkmcnt(5)
	v_pk_mul_f32 v[104:105], v[136:137], v[72:73] neg_lo:[1,0] neg_hi:[1,0]
	v_pk_mul_f32 v[106:107], v[138:139], v[74:75] neg_lo:[1,0] neg_hi:[1,0]
	v_pk_fma_f32 v[104:105], v[140:141], v[76:77], v[104:105] neg_lo:[1,0,0] neg_hi:[1,0,0]
	v_pk_fma_f32 v[106:107], v[142:143], v[78:79], v[106:107] neg_lo:[1,0,0] neg_hi:[1,0,0]
	v_pk_fma_f32 v[104:105], v[144:145], v[80:81], v[104:105] neg_lo:[1,0,0] neg_hi:[1,0,0]
	v_pk_fma_f32 v[106:107], v[146:147], v[82:83], v[106:107] neg_lo:[1,0,0] neg_hi:[1,0,0]
	v_pk_fma_f32 v[104:105], v[148:149], v[84:85], v[104:105] neg_lo:[1,0,0] neg_hi:[1,0,0]
	v_pk_fma_f32 v[106:107], v[150:151], v[86:87], v[106:107] neg_lo:[1,0,0] neg_hi:[1,0,0]
	v_pk_fma_f32 v[104:105], v[152:153], v[88:89], v[104:105] neg_lo:[1,0,0] neg_hi:[1,0,0]
	v_cndmask_b32_e64 v110, 0, 1.0, vcc
	v_pk_add_f32 v[104:105], v[104:105], v[106:107]
	v_add_f32_e32 v110, v110, v104
	v_add_f32_e32 v90, v110, v105
	v_cmp_eq_u32_e32 vcc, 19, v108
	ds_read_b128 v[136:139], v109 offset:5440
	ds_read_b128 v[140:143], v109 offset:5456
	ds_read_b128 v[144:147], v109 offset:5472
	ds_read_b128 v[148:151], v109 offset:5488
	ds_read_b128 v[152:155], v109 offset:5504
	s_waitcnt lgkmcnt(5)
	v_pk_mul_f32 v[104:105], v[168:169], v[72:73] neg_lo:[1,0] neg_hi:[1,0]
	v_pk_mul_f32 v[106:107], v[170:171], v[74:75] neg_lo:[1,0] neg_hi:[1,0]
	v_pk_fma_f32 v[104:105], v[172:173], v[76:77], v[104:105] neg_lo:[1,0,0] neg_hi:[1,0,0]
	v_pk_fma_f32 v[106:107], v[174:175], v[78:79], v[106:107] neg_lo:[1,0,0] neg_hi:[1,0,0]
	v_pk_fma_f32 v[104:105], v[176:177], v[80:81], v[104:105] neg_lo:[1,0,0] neg_hi:[1,0,0]
	v_pk_fma_f32 v[106:107], v[178:179], v[82:83], v[106:107] neg_lo:[1,0,0] neg_hi:[1,0,0]
	v_pk_fma_f32 v[104:105], v[180:181], v[84:85], v[104:105] neg_lo:[1,0,0] neg_hi:[1,0,0]
	v_pk_fma_f32 v[106:107], v[182:183], v[86:87], v[106:107] neg_lo:[1,0,0] neg_hi:[1,0,0]
	v_pk_fma_f32 v[104:105], v[184:185], v[88:89], v[104:105] neg_lo:[1,0,0] neg_hi:[1,0,0]
	v_cndmask_b32_e64 v110, 0, 1.0, vcc
	v_fma_f32 v110, -v186, v90, v110
	v_pk_add_f32 v[104:105], v[104:105], v[106:107]
	v_add_f32_e32 v110, v110, v104
	v_add_f32_e32 v91, v110, v105
	v_cmp_eq_u32_e32 vcc, 20, v108
	ds_read_b128 v[168:171], v109 offset:5712
	ds_read_b128 v[172:175], v109 offset:5728
	ds_read_b128 v[176:179], v109 offset:5744
	ds_read_b128 v[180:183], v109 offset:5760
	ds_read_b128 v[184:187], v109 offset:5776
	ds_read_b128 v[188:191], v109 offset:5792
	s_waitcnt lgkmcnt(6)
	v_pk_mul_f32 v[104:105], v[136:137], v[72:73] neg_lo:[1,0] neg_hi:[1,0]
	v_pk_mul_f32 v[106:107], v[138:139], v[74:75] neg_lo:[1,0] neg_hi:[1,0]
	v_pk_fma_f32 v[104:105], v[140:141], v[76:77], v[104:105] neg_lo:[1,0,0] neg_hi:[1,0,0]
	v_pk_fma_f32 v[106:107], v[142:143], v[78:79], v[106:107] neg_lo:[1,0,0] neg_hi:[1,0,0]
	v_pk_fma_f32 v[104:105], v[144:145], v[80:81], v[104:105] neg_lo:[1,0,0] neg_hi:[1,0,0]
	v_pk_fma_f32 v[106:107], v[146:147], v[82:83], v[106:107] neg_lo:[1,0,0] neg_hi:[1,0,0]
	v_pk_fma_f32 v[104:105], v[148:149], v[84:85], v[104:105] neg_lo:[1,0,0] neg_hi:[1,0,0]
	v_pk_fma_f32 v[106:107], v[150:151], v[86:87], v[106:107] neg_lo:[1,0,0] neg_hi:[1,0,0]
	v_pk_fma_f32 v[104:105], v[152:153], v[88:89], v[104:105] neg_lo:[1,0,0] neg_hi:[1,0,0]
	v_pk_fma_f32 v[106:107], v[154:155], v[90:91], v[106:107] neg_lo:[1,0,0] neg_hi:[1,0,0]
	v_cndmask_b32_e64 v110, 0, 1.0, vcc
	v_pk_add_f32 v[104:105], v[104:105], v[106:107]
	v_add_f32_e32 v110, v110, v104
	v_add_f32_e32 v92, v110, v105
	v_cmp_eq_u32_e32 vcc, 21, v108
	ds_read_b128 v[136:139], v109 offset:5984
	ds_read_b128 v[140:143], v109 offset:6000
	ds_read_b128 v[144:147], v109 offset:6016
	ds_read_b128 v[148:151], v109 offset:6032
	ds_read_b128 v[152:155], v109 offset:6048
	ds_read_b128 v[156:159], v109 offset:6064
	s_waitcnt lgkmcnt(6)
	v_pk_mul_f32 v[104:105], v[168:169], v[72:73] neg_lo:[1,0] neg_hi:[1,0]
	v_pk_mul_f32 v[106:107], v[170:171], v[74:75] neg_lo:[1,0] neg_hi:[1,0]
	v_pk_fma_f32 v[104:105], v[172:173], v[76:77], v[104:105] neg_lo:[1,0,0] neg_hi:[1,0,0]
	v_pk_fma_f32 v[106:107], v[174:175], v[78:79], v[106:107] neg_lo:[1,0,0] neg_hi:[1,0,0]
	v_pk_fma_f32 v[104:105], v[176:177], v[80:81], v[104:105] neg_lo:[1,0,0] neg_hi:[1,0,0]
	v_pk_fma_f32 v[106:107], v[178:179], v[82:83], v[106:107] neg_lo:[1,0,0] neg_hi:[1,0,0]
	v_pk_fma_f32 v[104:105], v[180:181], v[84:85], v[104:105] neg_lo:[1,0,0] neg_hi:[1,0,0]
	v_pk_fma_f32 v[106:107], v[182:183], v[86:87], v[106:107] neg_lo:[1,0,0] neg_hi:[1,0,0]
	v_pk_fma_f32 v[104:105], v[184:185], v[88:89], v[104:105] neg_lo:[1,0,0] neg_hi:[1,0,0]
	v_pk_fma_f32 v[106:107], v[186:187], v[90:91], v[106:107] neg_lo:[1,0,0] neg_hi:[1,0,0]
	v_cndmask_b32_e64 v110, 0, 1.0, vcc
	v_fma_f32 v110, -v188, v92, v110
	v_pk_add_f32 v[104:105], v[104:105], v[106:107]
	v_add_f32_e32 v110, v110, v104
	v_add_f32_e32 v93, v110, v105
	v_cmp_eq_u32_e32 vcc, 22, v108
	ds_read_b128 v[168:171], v109 offset:6256
	ds_read_b128 v[172:175], v109 offset:6272
	ds_read_b128 v[176:179], v109 offset:6288
	ds_read_b128 v[180:183], v109 offset:6304
	ds_read_b128 v[184:187], v109 offset:6320
	ds_read_b128 v[188:191], v109 offset:6336
	s_waitcnt lgkmcnt(6)
	v_pk_mul_f32 v[104:105], v[136:137], v[72:73] neg_lo:[1,0] neg_hi:[1,0]
	v_pk_mul_f32 v[106:107], v[138:139], v[74:75] neg_lo:[1,0] neg_hi:[1,0]
	v_pk_fma_f32 v[104:105], v[140:141], v[76:77], v[104:105] neg_lo:[1,0,0] neg_hi:[1,0,0]
	v_pk_fma_f32 v[106:107], v[142:143], v[78:79], v[106:107] neg_lo:[1,0,0] neg_hi:[1,0,0]
	v_pk_fma_f32 v[104:105], v[144:145], v[80:81], v[104:105] neg_lo:[1,0,0] neg_hi:[1,0,0]
	v_pk_fma_f32 v[106:107], v[146:147], v[82:83], v[106:107] neg_lo:[1,0,0] neg_hi:[1,0,0]
	v_pk_fma_f32 v[104:105], v[148:149], v[84:85], v[104:105] neg_lo:[1,0,0] neg_hi:[1,0,0]
	v_pk_fma_f32 v[106:107], v[150:151], v[86:87], v[106:107] neg_lo:[1,0,0] neg_hi:[1,0,0]
	v_pk_fma_f32 v[104:105], v[152:153], v[88:89], v[104:105] neg_lo:[1,0,0] neg_hi:[1,0,0]
	v_pk_fma_f32 v[106:107], v[154:155], v[90:91], v[106:107] neg_lo:[1,0,0] neg_hi:[1,0,0]
	v_pk_fma_f32 v[104:105], v[156:157], v[92:93], v[104:105] neg_lo:[1,0,0] neg_hi:[1,0,0]
	v_cndmask_b32_e64 v110, 0, 1.0, vcc
	v_pk_add_f32 v[104:105], v[104:105], v[106:107]
	v_add_f32_e32 v110, v110, v104
	v_add_f32_e32 v94, v110, v105
	v_cmp_eq_u32_e32 vcc, 23, v108
	ds_read_b128 v[136:139], v109 offset:6528
	ds_read_b128 v[140:143], v109 offset:6544
	ds_read_b128 v[144:147], v109 offset:6560
	ds_read_b128 v[148:151], v109 offset:6576
	ds_read_b128 v[152:155], v109 offset:6592
	ds_read_b128 v[156:159], v109 offset:6608
	s_waitcnt lgkmcnt(6)
	v_pk_mul_f32 v[104:105], v[168:169], v[72:73] neg_lo:[1,0] neg_hi:[1,0]
	v_pk_mul_f32 v[106:107], v[170:171], v[74:75] neg_lo:[1,0] neg_hi:[1,0]
	v_pk_fma_f32 v[104:105], v[172:173], v[76:77], v[104:105] neg_lo:[1,0,0] neg_hi:[1,0,0]
	v_pk_fma_f32 v[106:107], v[174:175], v[78:79], v[106:107] neg_lo:[1,0,0] neg_hi:[1,0,0]
	v_pk_fma_f32 v[104:105], v[176:177], v[80:81], v[104:105] neg_lo:[1,0,0] neg_hi:[1,0,0]
	v_pk_fma_f32 v[106:107], v[178:179], v[82:83], v[106:107] neg_lo:[1,0,0] neg_hi:[1,0,0]
	v_pk_fma_f32 v[104:105], v[180:181], v[84:85], v[104:105] neg_lo:[1,0,0] neg_hi:[1,0,0]
	v_pk_fma_f32 v[106:107], v[182:183], v[86:87], v[106:107] neg_lo:[1,0,0] neg_hi:[1,0,0]
	v_pk_fma_f32 v[104:105], v[184:185], v[88:89], v[104:105] neg_lo:[1,0,0] neg_hi:[1,0,0]
	v_pk_fma_f32 v[106:107], v[186:187], v[90:91], v[106:107] neg_lo:[1,0,0] neg_hi:[1,0,0]
	v_pk_fma_f32 v[104:105], v[188:189], v[92:93], v[104:105] neg_lo:[1,0,0] neg_hi:[1,0,0]
	v_cndmask_b32_e64 v110, 0, 1.0, vcc
	v_fma_f32 v110, -v190, v94, v110
	v_pk_add_f32 v[104:105], v[104:105], v[106:107]
	v_add_f32_e32 v110, v110, v104
	v_add_f32_e32 v95, v110, v105
	v_cmp_eq_u32_e32 vcc, 24, v108
	ds_read_b128 v[168:171], v109 offset:6800
	ds_read_b128 v[172:175], v109 offset:6816
	ds_read_b128 v[176:179], v109 offset:6832
	ds_read_b128 v[180:183], v109 offset:6848
	ds_read_b128 v[184:187], v109 offset:6864
	ds_read_b128 v[188:191], v109 offset:6880
	ds_read_b128 v[192:195], v109 offset:6896
	s_waitcnt lgkmcnt(7)
	v_pk_mul_f32 v[104:105], v[136:137], v[72:73] neg_lo:[1,0] neg_hi:[1,0]
	v_pk_mul_f32 v[106:107], v[138:139], v[74:75] neg_lo:[1,0] neg_hi:[1,0]
	v_pk_fma_f32 v[104:105], v[140:141], v[76:77], v[104:105] neg_lo:[1,0,0] neg_hi:[1,0,0]
	v_pk_fma_f32 v[106:107], v[142:143], v[78:79], v[106:107] neg_lo:[1,0,0] neg_hi:[1,0,0]
	v_pk_fma_f32 v[104:105], v[144:145], v[80:81], v[104:105] neg_lo:[1,0,0] neg_hi:[1,0,0]
	v_pk_fma_f32 v[106:107], v[146:147], v[82:83], v[106:107] neg_lo:[1,0,0] neg_hi:[1,0,0]
	v_pk_fma_f32 v[104:105], v[148:149], v[84:85], v[104:105] neg_lo:[1,0,0] neg_hi:[1,0,0]
	v_pk_fma_f32 v[106:107], v[150:151], v[86:87], v[106:107] neg_lo:[1,0,0] neg_hi:[1,0,0]
	v_pk_fma_f32 v[104:105], v[152:153], v[88:89], v[104:105] neg_lo:[1,0,0] neg_hi:[1,0,0]
	v_pk_fma_f32 v[106:107], v[154:155], v[90:91], v[106:107] neg_lo:[1,0,0] neg_hi:[1,0,0]
	v_pk_fma_f32 v[104:105], v[156:157], v[92:93], v[104:105] neg_lo:[1,0,0] neg_hi:[1,0,0]
	v_pk_fma_f32 v[106:107], v[158:159], v[94:95], v[106:107] neg_lo:[1,0,0] neg_hi:[1,0,0]
	v_cndmask_b32_e64 v110, 0, 1.0, vcc
	v_pk_add_f32 v[104:105], v[104:105], v[106:107]
	v_add_f32_e32 v110, v110, v104
	v_add_f32_e32 v96, v110, v105
	v_cmp_eq_u32_e32 vcc, 25, v108
	ds_read_b128 v[136:139], v109 offset:7072
	ds_read_b128 v[140:143], v109 offset:7088
	ds_read_b128 v[144:147], v109 offset:7104
	ds_read_b128 v[148:151], v109 offset:7120
	ds_read_b128 v[152:155], v109 offset:7136
	ds_read_b128 v[156:159], v109 offset:7152
	ds_read_b128 v[160:163], v109 offset:7168
	s_waitcnt lgkmcnt(7)
	v_pk_mul_f32 v[104:105], v[168:169], v[72:73] neg_lo:[1,0] neg_hi:[1,0]
	v_pk_mul_f32 v[106:107], v[170:171], v[74:75] neg_lo:[1,0] neg_hi:[1,0]
	v_pk_fma_f32 v[104:105], v[172:173], v[76:77], v[104:105] neg_lo:[1,0,0] neg_hi:[1,0,0]
	v_pk_fma_f32 v[106:107], v[174:175], v[78:79], v[106:107] neg_lo:[1,0,0] neg_hi:[1,0,0]
	v_pk_fma_f32 v[104:105], v[176:177], v[80:81], v[104:105] neg_lo:[1,0,0] neg_hi:[1,0,0]
	v_pk_fma_f32 v[106:107], v[178:179], v[82:83], v[106:107] neg_lo:[1,0,0] neg_hi:[1,0,0]
	v_pk_fma_f32 v[104:105], v[180:181], v[84:85], v[104:105] neg_lo:[1,0,0] neg_hi:[1,0,0]
	v_pk_fma_f32 v[106:107], v[182:183], v[86:87], v[106:107] neg_lo:[1,0,0] neg_hi:[1,0,0]
	v_pk_fma_f32 v[104:105], v[184:185], v[88:89], v[104:105] neg_lo:[1,0,0] neg_hi:[1,0,0]
	v_pk_fma_f32 v[106:107], v[186:187], v[90:91], v[106:107] neg_lo:[1,0,0] neg_hi:[1,0,0]
	v_pk_fma_f32 v[104:105], v[188:189], v[92:93], v[104:105] neg_lo:[1,0,0] neg_hi:[1,0,0]
	v_pk_fma_f32 v[106:107], v[190:191], v[94:95], v[106:107] neg_lo:[1,0,0] neg_hi:[1,0,0]
	v_cndmask_b32_e64 v110, 0, 1.0, vcc
	v_fma_f32 v110, -v192, v96, v110
	v_pk_add_f32 v[104:105], v[104:105], v[106:107]
	v_add_f32_e32 v110, v110, v104
	v_add_f32_e32 v97, v110, v105
	v_cmp_eq_u32_e32 vcc, 26, v108
	ds_read_b128 v[168:171], v109 offset:7344
	ds_read_b128 v[172:175], v109 offset:7360
	ds_read_b128 v[176:179], v109 offset:7376
	ds_read_b128 v[180:183], v109 offset:7392
	ds_read_b128 v[184:187], v109 offset:7408
	ds_read_b128 v[188:191], v109 offset:7424
	ds_read_b128 v[192:195], v109 offset:7440
	s_waitcnt lgkmcnt(7)
	v_pk_mul_f32 v[104:105], v[136:137], v[72:73] neg_lo:[1,0] neg_hi:[1,0]
	v_pk_mul_f32 v[106:107], v[138:139], v[74:75] neg_lo:[1,0] neg_hi:[1,0]
	v_pk_fma_f32 v[104:105], v[140:141], v[76:77], v[104:105] neg_lo:[1,0,0] neg_hi:[1,0,0]
	v_pk_fma_f32 v[106:107], v[142:143], v[78:79], v[106:107] neg_lo:[1,0,0] neg_hi:[1,0,0]
	v_pk_fma_f32 v[104:105], v[144:145], v[80:81], v[104:105] neg_lo:[1,0,0] neg_hi:[1,0,0]
	v_pk_fma_f32 v[106:107], v[146:147], v[82:83], v[106:107] neg_lo:[1,0,0] neg_hi:[1,0,0]
	v_pk_fma_f32 v[104:105], v[148:149], v[84:85], v[104:105] neg_lo:[1,0,0] neg_hi:[1,0,0]
	v_pk_fma_f32 v[106:107], v[150:151], v[86:87], v[106:107] neg_lo:[1,0,0] neg_hi:[1,0,0]
	v_pk_fma_f32 v[104:105], v[152:153], v[88:89], v[104:105] neg_lo:[1,0,0] neg_hi:[1,0,0]
	v_pk_fma_f32 v[106:107], v[154:155], v[90:91], v[106:107] neg_lo:[1,0,0] neg_hi:[1,0,0]
	v_pk_fma_f32 v[104:105], v[156:157], v[92:93], v[104:105] neg_lo:[1,0,0] neg_hi:[1,0,0]
	v_pk_fma_f32 v[106:107], v[158:159], v[94:95], v[106:107] neg_lo:[1,0,0] neg_hi:[1,0,0]
	v_pk_fma_f32 v[104:105], v[160:161], v[96:97], v[104:105] neg_lo:[1,0,0] neg_hi:[1,0,0]
	v_cndmask_b32_e64 v110, 0, 1.0, vcc
	v_pk_add_f32 v[104:105], v[104:105], v[106:107]
	v_add_f32_e32 v110, v110, v104
	v_add_f32_e32 v98, v110, v105
	v_cmp_eq_u32_e32 vcc, 27, v108
	ds_read_b128 v[136:139], v109 offset:7616
	ds_read_b128 v[140:143], v109 offset:7632
	ds_read_b128 v[144:147], v109 offset:7648
	ds_read_b128 v[148:151], v109 offset:7664
	ds_read_b128 v[152:155], v109 offset:7680
	ds_read_b128 v[156:159], v109 offset:7696
	ds_read_b128 v[160:163], v109 offset:7712
	s_waitcnt lgkmcnt(7)
	v_pk_mul_f32 v[104:105], v[168:169], v[72:73] neg_lo:[1,0] neg_hi:[1,0]
	v_pk_mul_f32 v[106:107], v[170:171], v[74:75] neg_lo:[1,0] neg_hi:[1,0]
	v_pk_fma_f32 v[104:105], v[172:173], v[76:77], v[104:105] neg_lo:[1,0,0] neg_hi:[1,0,0]
	v_pk_fma_f32 v[106:107], v[174:175], v[78:79], v[106:107] neg_lo:[1,0,0] neg_hi:[1,0,0]
	v_pk_fma_f32 v[104:105], v[176:177], v[80:81], v[104:105] neg_lo:[1,0,0] neg_hi:[1,0,0]
	v_pk_fma_f32 v[106:107], v[178:179], v[82:83], v[106:107] neg_lo:[1,0,0] neg_hi:[1,0,0]
	v_pk_fma_f32 v[104:105], v[180:181], v[84:85], v[104:105] neg_lo:[1,0,0] neg_hi:[1,0,0]
	v_pk_fma_f32 v[106:107], v[182:183], v[86:87], v[106:107] neg_lo:[1,0,0] neg_hi:[1,0,0]
	v_pk_fma_f32 v[104:105], v[184:185], v[88:89], v[104:105] neg_lo:[1,0,0] neg_hi:[1,0,0]
	v_pk_fma_f32 v[106:107], v[186:187], v[90:91], v[106:107] neg_lo:[1,0,0] neg_hi:[1,0,0]
	v_pk_fma_f32 v[104:105], v[188:189], v[92:93], v[104:105] neg_lo:[1,0,0] neg_hi:[1,0,0]
	v_pk_fma_f32 v[106:107], v[190:191], v[94:95], v[106:107] neg_lo:[1,0,0] neg_hi:[1,0,0]
	v_pk_fma_f32 v[104:105], v[192:193], v[96:97], v[104:105] neg_lo:[1,0,0] neg_hi:[1,0,0]
	v_cndmask_b32_e64 v110, 0, 1.0, vcc
	v_fma_f32 v110, -v194, v98, v110
	v_pk_add_f32 v[104:105], v[104:105], v[106:107]
	v_add_f32_e32 v110, v110, v104
	v_add_f32_e32 v99, v110, v105
	v_cmp_eq_u32_e32 vcc, 28, v108
	ds_read_b128 v[168:171], v109 offset:7888
	ds_read_b128 v[172:175], v109 offset:7904
	ds_read_b128 v[176:179], v109 offset:7920
	ds_read_b128 v[180:183], v109 offset:7936
	ds_read_b128 v[184:187], v109 offset:7952
	ds_read_b128 v[188:191], v109 offset:7968
	ds_read_b128 v[192:195], v109 offset:7984
	ds_read_b128 v[196:199], v109 offset:8000
	s_waitcnt lgkmcnt(8)
	v_pk_mul_f32 v[104:105], v[136:137], v[72:73] neg_lo:[1,0] neg_hi:[1,0]
	v_pk_mul_f32 v[106:107], v[138:139], v[74:75] neg_lo:[1,0] neg_hi:[1,0]
	v_pk_fma_f32 v[104:105], v[140:141], v[76:77], v[104:105] neg_lo:[1,0,0] neg_hi:[1,0,0]
	v_pk_fma_f32 v[106:107], v[142:143], v[78:79], v[106:107] neg_lo:[1,0,0] neg_hi:[1,0,0]
	v_pk_fma_f32 v[104:105], v[144:145], v[80:81], v[104:105] neg_lo:[1,0,0] neg_hi:[1,0,0]
	v_pk_fma_f32 v[106:107], v[146:147], v[82:83], v[106:107] neg_lo:[1,0,0] neg_hi:[1,0,0]
	v_pk_fma_f32 v[104:105], v[148:149], v[84:85], v[104:105] neg_lo:[1,0,0] neg_hi:[1,0,0]
	v_pk_fma_f32 v[106:107], v[150:151], v[86:87], v[106:107] neg_lo:[1,0,0] neg_hi:[1,0,0]
	v_pk_fma_f32 v[104:105], v[152:153], v[88:89], v[104:105] neg_lo:[1,0,0] neg_hi:[1,0,0]
	v_pk_fma_f32 v[106:107], v[154:155], v[90:91], v[106:107] neg_lo:[1,0,0] neg_hi:[1,0,0]
	v_pk_fma_f32 v[104:105], v[156:157], v[92:93], v[104:105] neg_lo:[1,0,0] neg_hi:[1,0,0]
	v_pk_fma_f32 v[106:107], v[158:159], v[94:95], v[106:107] neg_lo:[1,0,0] neg_hi:[1,0,0]
	v_pk_fma_f32 v[104:105], v[160:161], v[96:97], v[104:105] neg_lo:[1,0,0] neg_hi:[1,0,0]
	v_pk_fma_f32 v[106:107], v[162:163], v[98:99], v[106:107] neg_lo:[1,0,0] neg_hi:[1,0,0]
	v_cndmask_b32_e64 v110, 0, 1.0, vcc
	v_pk_add_f32 v[104:105], v[104:105], v[106:107]
	v_add_f32_e32 v110, v110, v104
	v_add_f32_e32 v100, v110, v105
	v_cmp_eq_u32_e32 vcc, 29, v108
	ds_read_b128 v[136:139], v109 offset:8160
	ds_read_b128 v[140:143], v109 offset:8176
	ds_read_b128 v[144:147], v109 offset:8192
	ds_read_b128 v[148:151], v109 offset:8208
	ds_read_b128 v[152:155], v109 offset:8224
	ds_read_b128 v[156:159], v109 offset:8240
	ds_read_b128 v[160:163], v109 offset:8256
	ds_read_b128 v[164:167], v109 offset:8272
	s_waitcnt lgkmcnt(8)
	v_pk_mul_f32 v[104:105], v[168:169], v[72:73] neg_lo:[1,0] neg_hi:[1,0]
	v_pk_mul_f32 v[106:107], v[170:171], v[74:75] neg_lo:[1,0] neg_hi:[1,0]
	v_pk_fma_f32 v[104:105], v[172:173], v[76:77], v[104:105] neg_lo:[1,0,0] neg_hi:[1,0,0]
	v_pk_fma_f32 v[106:107], v[174:175], v[78:79], v[106:107] neg_lo:[1,0,0] neg_hi:[1,0,0]
	v_pk_fma_f32 v[104:105], v[176:177], v[80:81], v[104:105] neg_lo:[1,0,0] neg_hi:[1,0,0]
	v_pk_fma_f32 v[106:107], v[178:179], v[82:83], v[106:107] neg_lo:[1,0,0] neg_hi:[1,0,0]
	v_pk_fma_f32 v[104:105], v[180:181], v[84:85], v[104:105] neg_lo:[1,0,0] neg_hi:[1,0,0]
	v_pk_fma_f32 v[106:107], v[182:183], v[86:87], v[106:107] neg_lo:[1,0,0] neg_hi:[1,0,0]
	v_pk_fma_f32 v[104:105], v[184:185], v[88:89], v[104:105] neg_lo:[1,0,0] neg_hi:[1,0,0]
	v_pk_fma_f32 v[106:107], v[186:187], v[90:91], v[106:107] neg_lo:[1,0,0] neg_hi:[1,0,0]
	v_pk_fma_f32 v[104:105], v[188:189], v[92:93], v[104:105] neg_lo:[1,0,0] neg_hi:[1,0,0]
	v_pk_fma_f32 v[106:107], v[190:191], v[94:95], v[106:107] neg_lo:[1,0,0] neg_hi:[1,0,0]
	v_pk_fma_f32 v[104:105], v[192:193], v[96:97], v[104:105] neg_lo:[1,0,0] neg_hi:[1,0,0]
	v_pk_fma_f32 v[106:107], v[194:195], v[98:99], v[106:107] neg_lo:[1,0,0] neg_hi:[1,0,0]
	v_cndmask_b32_e64 v110, 0, 1.0, vcc
	v_fma_f32 v110, -v196, v100, v110
	v_pk_add_f32 v[104:105], v[104:105], v[106:107]
	v_add_f32_e32 v110, v110, v104
	v_add_f32_e32 v101, v110, v105
	v_cmp_eq_u32_e32 vcc, 30, v108
	ds_read_b128 v[168:171], v109 offset:8432
	ds_read_b128 v[172:175], v109 offset:8448
	ds_read_b128 v[176:179], v109 offset:8464
	ds_read_b128 v[180:183], v109 offset:8480
	ds_read_b128 v[184:187], v109 offset:8496
	ds_read_b128 v[188:191], v109 offset:8512
	ds_read_b128 v[192:195], v109 offset:8528
	ds_read_b128 v[196:199], v109 offset:8544
	s_waitcnt lgkmcnt(8)
	v_pk_mul_f32 v[104:105], v[136:137], v[72:73] neg_lo:[1,0] neg_hi:[1,0]
	v_pk_mul_f32 v[106:107], v[138:139], v[74:75] neg_lo:[1,0] neg_hi:[1,0]
	v_pk_fma_f32 v[104:105], v[140:141], v[76:77], v[104:105] neg_lo:[1,0,0] neg_hi:[1,0,0]
	v_pk_fma_f32 v[106:107], v[142:143], v[78:79], v[106:107] neg_lo:[1,0,0] neg_hi:[1,0,0]
	v_pk_fma_f32 v[104:105], v[144:145], v[80:81], v[104:105] neg_lo:[1,0,0] neg_hi:[1,0,0]
	v_pk_fma_f32 v[106:107], v[146:147], v[82:83], v[106:107] neg_lo:[1,0,0] neg_hi:[1,0,0]
	v_pk_fma_f32 v[104:105], v[148:149], v[84:85], v[104:105] neg_lo:[1,0,0] neg_hi:[1,0,0]
	v_pk_fma_f32 v[106:107], v[150:151], v[86:87], v[106:107] neg_lo:[1,0,0] neg_hi:[1,0,0]
	v_pk_fma_f32 v[104:105], v[152:153], v[88:89], v[104:105] neg_lo:[1,0,0] neg_hi:[1,0,0]
	v_pk_fma_f32 v[106:107], v[154:155], v[90:91], v[106:107] neg_lo:[1,0,0] neg_hi:[1,0,0]
	v_pk_fma_f32 v[104:105], v[156:157], v[92:93], v[104:105] neg_lo:[1,0,0] neg_hi:[1,0,0]
	v_pk_fma_f32 v[106:107], v[158:159], v[94:95], v[106:107] neg_lo:[1,0,0] neg_hi:[1,0,0]
	v_pk_fma_f32 v[104:105], v[160:161], v[96:97], v[104:105] neg_lo:[1,0,0] neg_hi:[1,0,0]
	v_pk_fma_f32 v[106:107], v[162:163], v[98:99], v[106:107] neg_lo:[1,0,0] neg_hi:[1,0,0]
	v_pk_fma_f32 v[104:105], v[164:165], v[100:101], v[104:105] neg_lo:[1,0,0] neg_hi:[1,0,0]
	v_cndmask_b32_e64 v110, 0, 1.0, vcc
	v_pk_add_f32 v[104:105], v[104:105], v[106:107]
	v_add_f32_e32 v110, v110, v104
	v_add_f32_e32 v102, v110, v105
	v_cmp_eq_u32_e32 vcc, 31, v108
	s_nop 1
	s_waitcnt lgkmcnt(0)
	v_pk_mul_f32 v[104:105], v[168:169], v[72:73] neg_lo:[1,0] neg_hi:[1,0]
	v_pk_mul_f32 v[106:107], v[170:171], v[74:75] neg_lo:[1,0] neg_hi:[1,0]
	v_pk_fma_f32 v[104:105], v[172:173], v[76:77], v[104:105] neg_lo:[1,0,0] neg_hi:[1,0,0]
	v_pk_fma_f32 v[106:107], v[174:175], v[78:79], v[106:107] neg_lo:[1,0,0] neg_hi:[1,0,0]
	v_pk_fma_f32 v[104:105], v[176:177], v[80:81], v[104:105] neg_lo:[1,0,0] neg_hi:[1,0,0]
	v_pk_fma_f32 v[106:107], v[178:179], v[82:83], v[106:107] neg_lo:[1,0,0] neg_hi:[1,0,0]
	v_pk_fma_f32 v[104:105], v[180:181], v[84:85], v[104:105] neg_lo:[1,0,0] neg_hi:[1,0,0]
	v_pk_fma_f32 v[106:107], v[182:183], v[86:87], v[106:107] neg_lo:[1,0,0] neg_hi:[1,0,0]
	v_pk_fma_f32 v[104:105], v[184:185], v[88:89], v[104:105] neg_lo:[1,0,0] neg_hi:[1,0,0]
	v_pk_fma_f32 v[106:107], v[186:187], v[90:91], v[106:107] neg_lo:[1,0,0] neg_hi:[1,0,0]
	v_pk_fma_f32 v[104:105], v[188:189], v[92:93], v[104:105] neg_lo:[1,0,0] neg_hi:[1,0,0]
	v_pk_fma_f32 v[106:107], v[190:191], v[94:95], v[106:107] neg_lo:[1,0,0] neg_hi:[1,0,0]
	v_pk_fma_f32 v[104:105], v[192:193], v[96:97], v[104:105] neg_lo:[1,0,0] neg_hi:[1,0,0]
	v_pk_fma_f32 v[106:107], v[194:195], v[98:99], v[106:107] neg_lo:[1,0,0] neg_hi:[1,0,0]
	v_pk_fma_f32 v[104:105], v[196:197], v[100:101], v[104:105] neg_lo:[1,0,0] neg_hi:[1,0,0]
	v_cndmask_b32_e64 v110, 0, 1.0, vcc
	v_fma_f32 v110, -v198, v102, v110
	v_pk_add_f32 v[104:105], v[104:105], v[106:107]
	v_add_f32_e32 v110, v110, v104
	v_add_f32_e32 v103, v110, v105
	ds_write_b32 v1, v72 offset:0
	ds_write_b32 v1, v73 offset:128
	ds_write_b32 v1, v74 offset:256
	ds_write_b32 v1, v75 offset:384
	ds_write_b32 v1, v76 offset:512
	ds_write_b32 v1, v77 offset:640
	ds_write_b32 v1, v78 offset:768
	ds_write_b32 v1, v79 offset:896
	ds_write_b32 v1, v80 offset:1024
	ds_write_b32 v1, v81 offset:1152
	ds_write_b32 v1, v82 offset:1280
	ds_write_b32 v1, v83 offset:1408
	ds_write_b32 v1, v84 offset:1536
	ds_write_b32 v1, v85 offset:1664
	ds_write_b32 v1, v86 offset:1792
	ds_write_b32 v1, v87 offset:1920
	ds_write_b32 v1, v88 offset:2048
	ds_write_b32 v1, v89 offset:2176
	ds_write_b32 v1, v90 offset:2304
	ds_write_b32 v1, v91 offset:2432
	ds_write_b32 v1, v92 offset:2560
	ds_write_b32 v1, v93 offset:2688
	ds_write_b32 v1, v94 offset:2816
	ds_write_b32 v1, v95 offset:2944
	ds_write_b32 v1, v96 offset:3072
	ds_write_b32 v1, v97 offset:3200
	ds_write_b32 v1, v98 offset:3328
	ds_write_b32 v1, v99 offset:3456
	ds_write_b32 v1, v100 offset:3584
	ds_write_b32 v1, v101 offset:3712
	ds_write_b32 v1, v102 offset:3840
	ds_write_b32 v1, v103 offset:3968
.Lg4_s1done:
	s_waitcnt lgkmcnt(0)
	s_barrier
	s_lshr_b32 s1, s10, 2
	s_and_b32 s11, s10, 3
	v_lshrrev_b32_e32 v4, 5, v21
	v_and_b32_e32 v108, 31, v21
	s_mul_i32 s12, s1, 0x3000
	v_lshl_add_u32 v4, s11, 1, v4
	s_mul_i32 s13, s1, 0x4800
	s_add_i32 s12, s12, 0x1b000
	v_lshlrev_b32_e32 v5, 2, v108
	v_mul_u32_u24_e32 v6, 0x440, v4
	v_lshlrev_b32_e32 v7, 9, v4
	v_add3_u32 v8, v61, v5, s12
	s_add_i32 s24, s13, 0x2200
	v_add3_u32 v9, v61, v6, s24
	v_add_u32_e32 v10, v8, v7
	v_add3_u32 v11, v61, v7, s12
	ds_read_b32 v200, v8 offset:0
	ds_read_b32 v201, v8 offset:128
	ds_read_b32 v202, v8 offset:256
	ds_read_b32 v203, v8 offset:384
	ds_read_b32 v204, v8 offset:512
	ds_read_b32 v205, v8 offset:640
	ds_read_b32 v206, v8 offset:768
	ds_read_b32 v207, v8 offset:896
	ds_read_b32 v208, v8 offset:1024
	ds_read_b32 v209, v8 offset:1152
	ds_read_b32 v210, v8 offset:1280
	ds_read_b32 v211, v8 offset:1408
	ds_read_b32 v212, v8 offset:1536
	ds_read_b32 v213, v8 offset:1664
	ds_read_b32 v214, v8 offset:1792
	ds_read_b32 v215, v8 offset:1920
	ds_read_b32 v216, v8 offset:2048
	ds_read_b32 v217, v8 offset:2176
	ds_read_b32 v218, v8 offset:2304
	ds_read_b32 v219, v8 offset:2432
	ds_read_b32 v220, v8 offset:2560
	ds_read_b32 v221, v8 offset:2688
	ds_read_b32 v222, v8 offset:2816
	ds_read_b32 v223, v8 offset:2944
	ds_read_b32 v224, v8 offset:3072
	ds_read_b32 v225, v8 offset:3200
	ds_read_b32 v226, v8 offset:3328
	ds_read_b32 v227, v8 offset:3456
	ds_read_b32 v228, v8 offset:3584
	ds_read_b32 v229, v8 offset:3712
	ds_read_b32 v230, v8 offset:3840
	ds_read_b32 v231, v8 offset:3968
	ds_read_b128 v[136:139], v9 offset:0
	ds_read_b128 v[140:143], v9 offset:16
	ds_read_b128 v[144:147], v9 offset:32
	ds_read_b128 v[148:151], v9 offset:48
	ds_read_b128 v[152:155], v9 offset:64
	ds_read_b128 v[156:159], v9 offset:80
	ds_read_b128 v[160:163], v9 offset:96
	ds_read_b128 v[164:167], v9 offset:112
	s_waitcnt lgkmcnt(0)
	ds_read_b128 v[168:171], v9 offset:272
	ds_read_b128 v[172:175], v9 offset:288
	ds_read_b128 v[176:179], v9 offset:304
	ds_read_b128 v[180:183], v9 offset:320
	ds_read_b128 v[184:187], v9 offset:336
	ds_read_b128 v[188:191], v9 offset:352
	ds_read_b128 v[192:195], v9 offset:368
	ds_read_b128 v[196:199], v9 offset:384
	v_pk_mul_f32 v[104:105], v[136:137], v[200:201]
	v_pk_mul_f32 v[106:107], v[138:139], v[202:203]
	v_pk_fma_f32 v[104:105], v[140:141], v[204:205], v[104:105]
	v_pk_fma_f32 v[106:107], v[142:143], v[206:207], v[106:107]
	v_pk_fma_f32 v[104:105], v[144:145], v[208:209], v[104:105]
	v_pk_fma_f32 v[106:107], v[146:147], v[210:211], v[106:107]
	v_pk_fma_f32 v[104:105], v[148:149], v[212:213], v[104:105]
	v_pk_fma_f32 v[106:107], v[150:151], v[214:215], v[106:107]
	v_pk_fma_f32 v[104:105], v[152:153], v[216:217], v[104:105]
	v_pk_fma_f32 v[106:107], v[154:155], v[218:219], v[106:107]
	v_pk_fma_f32 v[104:105], v[156:157], v[220:221], v[104:105]
	v_pk_fma_f32 v[106:107], v[158:159], v[222:223], v[106:107]
	v_pk_fma_f32 v[104:105], v[160:161], v[224:225], v[104:105]
	v_pk_fma_f32 v[106:107], v[162:163], v[226:227], v[106:107]
	v_pk_fma_f32 v[104:105], v[164:165], v[228:229], v[104:105]
	v_pk_fma_f32 v[106:107], v[166:167], v[230:231], v[106:107]
	v_pk_add_f32 v[104:105], v[104:105], v[106:107]
	s_nop 0
	v_add_f32_e32 v232, v104, v105
	s_waitcnt lgkmcnt(0)
	ds_read_b128 v[136:139], v9 offset:544
	ds_read_b128 v[140:143], v9 offset:560
	ds_read_b128 v[144:147], v9 offset:576
	ds_read_b128 v[148:151], v9 offset:592
	ds_read_b128 v[152:155], v9 offset:608
	ds_read_b128 v[156:159], v9 offset:624
	ds_read_b128 v[160:163], v9 offset:640
	ds_read_b128 v[164:167], v9 offset:656
	v_pk_mul_f32 v[104:105], v[168:169], v[200:201]
	v_pk_mul_f32 v[106:107], v[170:171], v[202:203]
	v_pk_fma_f32 v[104:105], v[172:173], v[204:205], v[104:105]
	v_pk_fma_f32 v[106:107], v[174:175], v[206:207], v[106:107]
	v_pk_fma_f32 v[104:105], v[176:177], v[208:209], v[104:105]
	v_pk_fma_f32 v[106:107], v[178:179], v[210:211], v[106:107]
	v_pk_fma_f32 v[104:105], v[180:181], v[212:213], v[104:105]
	v_pk_fma_f32 v[106:107], v[182:183], v[214:215], v[106:107]
	v_pk_fma_f32 v[104:105], v[184:185], v[216:217], v[104:105]
	v_pk_fma_f32 v[106:107], v[186:187], v[218:219], v[106:107]
	v_pk_fma_f32 v[104:105], v[188:189], v[220:221], v[104:105]
	v_pk_fma_f32 v[106:107], v[190:191], v[222:223], v[106:107]
	v_pk_fma_f32 v[104:105], v[192:193], v[224:225], v[104:105]
	v_pk_fma_f32 v[106:107], v[194:195], v[226:227], v[106:107]
	v_pk_fma_f32 v[104:105], v[196:197], v[228:229], v[104:105]
	v_pk_fma_f32 v[106:107], v[198:199], v[230:231], v[106:107]
	v_pk_add_f32 v[104:105], v[104:105], v[106:107]
	s_nop 0
	v_add_f32_e32 v233, v104, v105
	s_waitcnt lgkmcnt(0)
	ds_read_b128 v[168:171], v9 offset:816
	ds_read_b128 v[172:175], v9 offset:832
	ds_read_b128 v[176:179], v9 offset:848
	ds_read_b128 v[180:183], v9 offset:864
	ds_read_b128 v[184:187], v9 offset:880
	ds_read_b128 v[188:191], v9 offset:896
	ds_read_b128 v[192:195], v9 offset:912
	ds_read_b128 v[196:199], v9 offset:928
	v_pk_mul_f32 v[104:105], v[136:137], v[200:201]
	v_pk_mul_f32 v[106:107], v[138:139], v[202:203]
	v_pk_fma_f32 v[104:105], v[140:141], v[204:205], v[104:105]
	v_pk_fma_f32 v[106:107], v[142:143], v[206:207], v[106:107]
	v_pk_fma_f32 v[104:105], v[144:145], v[208:209], v[104:105]
	v_pk_fma_f32 v[106:107], v[146:147], v[210:211], v[106:107]
	v_pk_fma_f32 v[104:105], v[148:149], v[212:213], v[104:105]
	v_pk_fma_f32 v[106:107], v[150:151], v[214:215], v[106:107]
	v_pk_fma_f32 v[104:105], v[152:153], v[216:217], v[104:105]
	v_pk_fma_f32 v[106:107], v[154:155], v[218:219], v[106:107]
	v_pk_fma_f32 v[104:105], v[156:157], v[220:221], v[104:105]
	v_pk_fma_f32 v[106:107], v[158:159], v[222:223], v[106:107]
	v_pk_fma_f32 v[104:105], v[160:161], v[224:225], v[104:105]
	v_pk_fma_f32 v[106:107], v[162:163], v[226:227], v[106:107]
	v_pk_fma_f32 v[104:105], v[164:165], v[228:229], v[104:105]
	v_pk_fma_f32 v[106:107], v[166:167], v[230:231], v[106:107]
	v_pk_add_f32 v[104:105], v[104:105], v[106:107]
	s_nop 0
	v_add_f32_e32 v234, v104, v105
	s_waitcnt lgkmcnt(0)
	v_pk_mul_f32 v[104:105], v[168:169], v[200:201]
	v_pk_mul_f32 v[106:107], v[170:171], v[202:203]
	v_pk_fma_f32 v[104:105], v[172:173], v[204:205], v[104:105]
	v_pk_fma_f32 v[106:107], v[174:175], v[206:207], v[106:107]
	v_pk_fma_f32 v[104:105], v[176:177], v[208:209], v[104:105]
	v_pk_fma_f32 v[106:107], v[178:179], v[210:211], v[106:107]
	v_pk_fma_f32 v[104:105], v[180:181], v[212:213], v[104:105]
	v_pk_fma_f32 v[106:107], v[182:183], v[214:215], v[106:107]
	v_pk_fma_f32 v[104:105], v[184:185], v[216:217], v[104:105]
	v_pk_fma_f32 v[106:107], v[186:187], v[218:219], v[106:107]
	v_pk_fma_f32 v[104:105], v[188:189], v[220:221], v[104:105]
	v_pk_fma_f32 v[106:107], v[190:191], v[222:223], v[106:107]
	v_pk_fma_f32 v[104:105], v[192:193], v[224:225], v[104:105]
	v_pk_fma_f32 v[106:107], v[194:195], v[226:227], v[106:107]
	v_pk_fma_f32 v[104:105], v[196:197], v[228:229], v[104:105]
	v_pk_fma_f32 v[106:107], v[198:199], v[230:231], v[106:107]
	v_pk_add_f32 v[104:105], v[104:105], v[106:107]
	s_nop 0
	v_add_f32_e32 v235, v104, v105
	ds_write_b32 v10, v232 offset:8192
	ds_write_b32 v10, v233 offset:8320
	ds_write_b32 v10, v234 offset:8448
	ds_write_b32 v10, v235 offset:8576
	s_waitcnt lgkmcnt(0)
	s_barrier
	ds_read_b32 v200, v8 offset:8192
	ds_read_b32 v201, v8 offset:8320
	ds_read_b32 v202, v8 offset:8448
	ds_read_b32 v203, v8 offset:8576
	ds_read_b32 v204, v8 offset:8704
	ds_read_b32 v205, v8 offset:8832
	ds_read_b32 v206, v8 offset:8960
	ds_read_b32 v207, v8 offset:9088
	ds_read_b32 v208, v8 offset:9216
	ds_read_b32 v209, v8 offset:9344
	ds_read_b32 v210, v8 offset:9472
	ds_read_b32 v211, v8 offset:9600
	ds_read_b32 v212, v8 offset:9728
	ds_read_b32 v213, v8 offset:9856
	ds_read_b32 v214, v8 offset:9984
	ds_read_b32 v215, v8 offset:10112
	ds_read_b32 v216, v8 offset:10240
	ds_read_b32 v217, v8 offset:10368
	ds_read_b32 v218, v8 offset:10496
	ds_read_b32 v219, v8 offset:10624
	ds_read_b32 v220, v8 offset:10752
	ds_read_b32 v221, v8 offset:10880
	ds_read_b32 v222, v8 offset:11008
	ds_read_b32 v223, v8 offset:11136
	ds_read_b32 v224, v8 offset:11264
	ds_read_b32 v225, v8 offset:11392
	ds_read_b32 v226, v8 offset:11520
	ds_read_b32 v227, v8 offset:11648
	ds_read_b32 v228, v8 offset:11776
	ds_read_b32 v229, v8 offset:11904
	ds_read_b32 v230, v8 offset:12032
	ds_read_b32 v231, v8 offset:12160
	ds_read_b128 v[136:139], v11 offset:4096
	ds_read_b128 v[140:143], v11 offset:4112
	ds_read_b128 v[144:147], v11 offset:4128
	ds_read_b128 v[148:151], v11 offset:4144
	ds_read_b128 v[152:155], v11 offset:4160
	ds_read_b128 v[156:159], v11 offset:4176
	ds_read_b128 v[160:163], v11 offset:4192
	ds_read_b128 v[164:167], v11 offset:4208
	s_waitcnt lgkmcnt(0)
	ds_read_b128 v[168:171], v11 offset:4224
	ds_read_b128 v[172:175], v11 offset:4240
	ds_read_b128 v[176:179], v11 offset:4256
	ds_read_b128 v[180:183], v11 offset:4272
	ds_read_b128 v[184:187], v11 offset:4288
	ds_read_b128 v[188:191], v11 offset:4304
	ds_read_b128 v[192:195], v11 offset:4320
	ds_read_b128 v[196:199], v11 offset:4336
	v_pk_mul_f32 v[104:105], v[136:137], v[200:201]
	v_pk_mul_f32 v[106:107], v[138:139], v[202:203]
	v_pk_fma_f32 v[104:105], v[140:141], v[204:205], v[104:105]
	v_pk_fma_f32 v[106:107], v[142:143], v[206:207], v[106:107]
	v_pk_fma_f32 v[104:105], v[144:145], v[208:209], v[104:105]
	v_pk_fma_f32 v[106:107], v[146:147], v[210:211], v[106:107]
	v_pk_fma_f32 v[104:105], v[148:149], v[212:213], v[104:105]
	v_pk_fma_f32 v[106:107], v[150:151], v[214:215], v[106:107]
	v_pk_fma_f32 v[104:105], v[152:153], v[216:217], v[104:105]
	v_pk_fma_f32 v[106:107], v[154:155], v[218:219], v[106:107]
	v_pk_fma_f32 v[104:105], v[156:157], v[220:221], v[104:105]
	v_pk_fma_f32 v[106:107], v[158:159], v[222:223], v[106:107]
	v_pk_fma_f32 v[104:105], v[160:161], v[224:225], v[104:105]
	v_pk_fma_f32 v[106:107], v[162:163], v[226:227], v[106:107]
	v_pk_fma_f32 v[104:105], v[164:165], v[228:229], v[104:105]
	v_pk_fma_f32 v[106:107], v[166:167], v[230:231], v[106:107]
	v_pk_add_f32 v[104:105], v[104:105], v[106:107]
	s_nop 0
	v_add_f32_e32 v232, v104, v105
	s_waitcnt lgkmcnt(0)
	ds_read_b128 v[136:139], v11 offset:4352
	ds_read_b128 v[140:143], v11 offset:4368
	ds_read_b128 v[144:147], v11 offset:4384
	ds_read_b128 v[148:151], v11 offset:4400
	ds_read_b128 v[152:155], v11 offset:4416
	ds_read_b128 v[156:159], v11 offset:4432
	ds_read_b128 v[160:163], v11 offset:4448
	ds_read_b128 v[164:167], v11 offset:4464
	v_pk_mul_f32 v[104:105], v[168:169], v[200:201]
	v_pk_mul_f32 v[106:107], v[170:171], v[202:203]
	v_pk_fma_f32 v[104:105], v[172:173], v[204:205], v[104:105]
	v_pk_fma_f32 v[106:107], v[174:175], v[206:207], v[106:107]
	v_pk_fma_f32 v[104:105], v[176:177], v[208:209], v[104:105]
	v_pk_fma_f32 v[106:107], v[178:179], v[210:211], v[106:107]
	v_pk_fma_f32 v[104:105], v[180:181], v[212:213], v[104:105]
	v_pk_fma_f32 v[106:107], v[182:183], v[214:215], v[106:107]
	v_pk_fma_f32 v[104:105], v[184:185], v[216:217], v[104:105]
	v_pk_fma_f32 v[106:107], v[186:187], v[218:219], v[106:107]
	v_pk_fma_f32 v[104:105], v[188:189], v[220:221], v[104:105]
	v_pk_fma_f32 v[106:107], v[190:191], v[222:223], v[106:107]
	v_pk_fma_f32 v[104:105], v[192:193], v[224:225], v[104:105]
	v_pk_fma_f32 v[106:107], v[194:195], v[226:227], v[106:107]
	v_pk_fma_f32 v[104:105], v[196:197], v[228:229], v[104:105]
	v_pk_fma_f32 v[106:107], v[198:199], v[230:231], v[106:107]
	v_pk_add_f32 v[104:105], v[104:105], v[106:107]
	s_nop 0
	v_add_f32_e32 v233, v104, v105
	s_waitcnt lgkmcnt(0)
	ds_read_b128 v[168:171], v11 offset:4480
	ds_read_b128 v[172:175], v11 offset:4496
	ds_read_b128 v[176:179], v11 offset:4512
	ds_read_b128 v[180:183], v11 offset:4528
	ds_read_b128 v[184:187], v11 offset:4544
	ds_read_b128 v[188:191], v11 offset:4560
	ds_read_b128 v[192:195], v11 offset:4576
	ds_read_b128 v[196:199], v11 offset:4592
	v_pk_mul_f32 v[104:105], v[136:137], v[200:201]
	v_pk_mul_f32 v[106:107], v[138:139], v[202:203]
	v_pk_fma_f32 v[104:105], v[140:141], v[204:205], v[104:105]
	v_pk_fma_f32 v[106:107], v[142:143], v[206:207], v[106:107]
	v_pk_fma_f32 v[104:105], v[144:145], v[208:209], v[104:105]
	v_pk_fma_f32 v[106:107], v[146:147], v[210:211], v[106:107]
	v_pk_fma_f32 v[104:105], v[148:149], v[212:213], v[104:105]
	v_pk_fma_f32 v[106:107], v[150:151], v[214:215], v[106:107]
	v_pk_fma_f32 v[104:105], v[152:153], v[216:217], v[104:105]
	v_pk_fma_f32 v[106:107], v[154:155], v[218:219], v[106:107]
	v_pk_fma_f32 v[104:105], v[156:157], v[220:221], v[104:105]
	v_pk_fma_f32 v[106:107], v[158:159], v[222:223], v[106:107]
	v_pk_fma_f32 v[104:105], v[160:161], v[224:225], v[104:105]
	v_pk_fma_f32 v[106:107], v[162:163], v[226:227], v[106:107]
	v_pk_fma_f32 v[104:105], v[164:165], v[228:229], v[104:105]
	v_pk_fma_f32 v[106:107], v[166:167], v[230:231], v[106:107]
	v_pk_add_f32 v[104:105], v[104:105], v[106:107]
	s_nop 0
	v_add_f32_e32 v234, v104, v105
	s_waitcnt lgkmcnt(0)
	v_pk_mul_f32 v[104:105], v[168:169], v[200:201]
	v_pk_mul_f32 v[106:107], v[170:171], v[202:203]
	v_pk_fma_f32 v[104:105], v[172:173], v[204:205], v[104:105]
	v_pk_fma_f32 v[106:107], v[174:175], v[206:207], v[106:107]
	v_pk_fma_f32 v[104:105], v[176:177], v[208:209], v[104:105]
	v_pk_fma_f32 v[106:107], v[178:179], v[210:211], v[106:107]
	v_pk_fma_f32 v[104:105], v[180:181], v[212:213], v[104:105]
	v_pk_fma_f32 v[106:107], v[182:183], v[214:215], v[106:107]
	v_pk_fma_f32 v[104:105], v[184:185], v[216:217], v[104:105]
	v_pk_fma_f32 v[106:107], v[186:187], v[218:219], v[106:107]
	v_pk_fma_f32 v[104:105], v[188:189], v[220:221], v[104:105]
	v_pk_fma_f32 v[106:107], v[190:191], v[222:223], v[106:107]
	v_pk_fma_f32 v[104:105], v[192:193], v[224:225], v[104:105]
	v_pk_fma_f32 v[106:107], v[194:195], v[226:227], v[106:107]
	v_pk_fma_f32 v[104:105], v[196:197], v[228:229], v[104:105]
	v_pk_fma_f32 v[106:107], v[198:199], v[230:231], v[106:107]
	v_pk_add_f32 v[104:105], v[104:105], v[106:107]
	s_nop 0
	v_add_f32_e32 v235, v104, v105
	s_lshl_b32 s24, s1, 8
	s_add_i32 s24, s24, 0x23200
	v_add3_u32 v12, v61, v5, s24
	ds_read_b32 v13, v12
	ds_read_b32 v14, v12 offset:512
	v_mul_u32_u24_e32 v15, 0x240, v4
	s_add_i32 s24, s13, 0x1200
	v_lshl_add_u32 v15, v108, 1, v15
	v_add3_u32 v15, v61, v15, s24
	s_waitcnt lgkmcnt(0)
	v_mul_f32_e32 v13, 0x3fb8aa3b, v13
	v_exp_f32_e32 v13, v13
	s_nop 0
	v_mul_f32_e32 v13, v14, v13
	v_mul_f32_e64 v16, -v232, v13
	v_mul_f32_e64 v17, -v232, v14
	v_cvt_pk_bf16_f32 v16, v16, v16
	v_cvt_pk_bf16_f32 v17, v17, v17
	ds_write_b16 v15, v16 offset:0
	ds_write_b16 v15, v17 offset:9216
	v_mul_f32_e64 v16, -v233, v13
	v_mul_f32_e64 v17, -v233, v14
	v_cvt_pk_bf16_f32 v16, v16, v16
	v_cvt_pk_bf16_f32 v17, v17, v17
	ds_write_b16 v15, v16 offset:144
	ds_write_b16 v15, v17 offset:9360
	v_mul_f32_e64 v16, -v234, v13
	v_mul_f32_e64 v17, -v234, v14
	v_cvt_pk_bf16_f32 v16, v16, v16
	v_cvt_pk_bf16_f32 v17, v17, v17
	ds_write_b16 v15, v16 offset:288
	ds_write_b16 v15, v17 offset:9504
	v_mul_f32_e64 v16, -v235, v13
	v_mul_f32_e64 v17, -v235, v14
	v_cvt_pk_bf16_f32 v16, v16, v16
	v_cvt_pk_bf16_f32 v17, v17, v17
	ds_write_b16 v15, v16 offset:432
	ds_write_b16 v15, v17 offset:9648
	s_cmp_gt_u32 s10, 1
	s_cbranch_scc1 .Lg4_done
	s_lshl_b32 s24, s10, 8
	v_lshlrev_b32_e32 v5, 2, v21
	s_add_i32 s24, s24, 0x23200
	v_lshrrev_b32_e32 v4, 5, v21
	v_add3_u32 v12, v61, v5, s24
	ds_read_b32 v13, v12
	ds_read_b32 v14, v12 offset:512
	v_mul_u32_u24_e32 v6, 0x1200, v4
	s_mul_i32 s24, s10, 0x4800
	v_lshl_add_u32 v6, v21, 1, v6
	v_add3_u32 v15, v61, v6, s24
	s_waitcnt lgkmcnt(0)
	v_mul_f32_e32 v13, 0x3fb8aa3b, v13
	v_exp_f32_e32 v13, v13
	s_nop 0
	v_mul_f32_e32 v13, v14, v13
	v_mul_f32_e32 v16, v72, v13
	v_mul_f32_e32 v17, v72, v14
	v_cvt_pk_bf16_f32 v16, v16, v16
	v_cvt_pk_bf16_f32 v17, v17, v17
	ds_write_b16 v15, v16 offset:0
	ds_write_b16 v15, v17 offset:9216
	v_mul_f32_e32 v16, v73, v13
	v_mul_f32_e32 v17, v73, v14
	v_cvt_pk_bf16_f32 v16, v16, v16
	v_cvt_pk_bf16_f32 v17, v17, v17
	ds_write_b16 v15, v16 offset:144
	ds_write_b16 v15, v17 offset:9360
	v_mul_f32_e32 v16, v74, v13
	v_mul_f32_e32 v17, v74, v14
	v_cvt_pk_bf16_f32 v16, v16, v16
	v_cvt_pk_bf16_f32 v17, v17, v17
	ds_write_b16 v15, v16 offset:288
	ds_write_b16 v15, v17 offset:9504
	v_mul_f32_e32 v16, v75, v13
	v_mul_f32_e32 v17, v75, v14
	v_cvt_pk_bf16_f32 v16, v16, v16
	v_cvt_pk_bf16_f32 v17, v17, v17
	ds_write_b16 v15, v16 offset:432
	ds_write_b16 v15, v17 offset:9648
	v_mul_f32_e32 v16, v76, v13
	v_mul_f32_e32 v17, v76, v14
	v_cvt_pk_bf16_f32 v16, v16, v16
	v_cvt_pk_bf16_f32 v17, v17, v17
	ds_write_b16 v15, v16 offset:576
	ds_write_b16 v15, v17 offset:9792
	v_mul_f32_e32 v16, v77, v13
	v_mul_f32_e32 v17, v77, v14
	v_cvt_pk_bf16_f32 v16, v16, v16
	v_cvt_pk_bf16_f32 v17, v17, v17
	ds_write_b16 v15, v16 offset:720
	ds_write_b16 v15, v17 offset:9936
	v_mul_f32_e32 v16, v78, v13
	v_mul_f32_e32 v17, v78, v14
	v_cvt_pk_bf16_f32 v16, v16, v16
	v_cvt_pk_bf16_f32 v17, v17, v17
	ds_write_b16 v15, v16 offset:864
	ds_write_b16 v15, v17 offset:10080
	v_mul_f32_e32 v16, v79, v13
	v_mul_f32_e32 v17, v79, v14
	v_cvt_pk_bf16_f32 v16, v16, v16
	v_cvt_pk_bf16_f32 v17, v17, v17
	ds_write_b16 v15, v16 offset:1008
	ds_write_b16 v15, v17 offset:10224
	v_mul_f32_e32 v16, v80, v13
	v_mul_f32_e32 v17, v80, v14
	v_cvt_pk_bf16_f32 v16, v16, v16
	v_cvt_pk_bf16_f32 v17, v17, v17
	ds_write_b16 v15, v16 offset:1152
	ds_write_b16 v15, v17 offset:10368
	v_mul_f32_e32 v16, v81, v13
	v_mul_f32_e32 v17, v81, v14
	v_cvt_pk_bf16_f32 v16, v16, v16
	v_cvt_pk_bf16_f32 v17, v17, v17
	ds_write_b16 v15, v16 offset:1296
	ds_write_b16 v15, v17 offset:10512
	v_mul_f32_e32 v16, v82, v13
	v_mul_f32_e32 v17, v82, v14
	v_cvt_pk_bf16_f32 v16, v16, v16
	v_cvt_pk_bf16_f32 v17, v17, v17
	ds_write_b16 v15, v16 offset:1440
	ds_write_b16 v15, v17 offset:10656
	v_mul_f32_e32 v16, v83, v13
	v_mul_f32_e32 v17, v83, v14
	v_cvt_pk_bf16_f32 v16, v16, v16
	v_cvt_pk_bf16_f32 v17, v17, v17
	ds_write_b16 v15, v16 offset:1584
	ds_write_b16 v15, v17 offset:10800
	v_mul_f32_e32 v16, v84, v13
	v_mul_f32_e32 v17, v84, v14
	v_cvt_pk_bf16_f32 v16, v16, v16
	v_cvt_pk_bf16_f32 v17, v17, v17
	ds_write_b16 v15, v16 offset:1728
	ds_write_b16 v15, v17 offset:10944
	v_mul_f32_e32 v16, v85, v13
	v_mul_f32_e32 v17, v85, v14
	v_cvt_pk_bf16_f32 v16, v16, v16
	v_cvt_pk_bf16_f32 v17, v17, v17
	ds_write_b16 v15, v16 offset:1872
	ds_write_b16 v15, v17 offset:11088
	v_mul_f32_e32 v16, v86, v13
	v_mul_f32_e32 v17, v86, v14
	v_cvt_pk_bf16_f32 v16, v16, v16
	v_cvt_pk_bf16_f32 v17, v17, v17
	ds_write_b16 v15, v16 offset:2016
	ds_write_b16 v15, v17 offset:11232
	v_mul_f32_e32 v16, v87, v13
	v_mul_f32_e32 v17, v87, v14
	v_cvt_pk_bf16_f32 v16, v16, v16
	v_cvt_pk_bf16_f32 v17, v17, v17
	ds_write_b16 v15, v16 offset:2160
	ds_write_b16 v15, v17 offset:11376
	v_mul_f32_e32 v16, v88, v13
	v_mul_f32_e32 v17, v88, v14
	v_cvt_pk_bf16_f32 v16, v16, v16
	v_cvt_pk_bf16_f32 v17, v17, v17
	ds_write_b16 v15, v16 offset:2304
	ds_write_b16 v15, v17 offset:11520
	v_mul_f32_e32 v16, v89, v13
	v_mul_f32_e32 v17, v89, v14
	v_cvt_pk_bf16_f32 v16, v16, v16
	v_cvt_pk_bf16_f32 v17, v17, v17
	ds_write_b16 v15, v16 offset:2448
	ds_write_b16 v15, v17 offset:11664
	v_mul_f32_e32 v16, v90, v13
	v_mul_f32_e32 v17, v90, v14
	v_cvt_pk_bf16_f32 v16, v16, v16
	v_cvt_pk_bf16_f32 v17, v17, v17
	ds_write_b16 v15, v16 offset:2592
	ds_write_b16 v15, v17 offset:11808
	v_mul_f32_e32 v16, v91, v13
	v_mul_f32_e32 v17, v91, v14
	v_cvt_pk_bf16_f32 v16, v16, v16
	v_cvt_pk_bf16_f32 v17, v17, v17
	ds_write_b16 v15, v16 offset:2736
	ds_write_b16 v15, v17 offset:11952
	v_mul_f32_e32 v16, v92, v13
	v_mul_f32_e32 v17, v92, v14
	v_cvt_pk_bf16_f32 v16, v16, v16
	v_cvt_pk_bf16_f32 v17, v17, v17
	ds_write_b16 v15, v16 offset:2880
	ds_write_b16 v15, v17 offset:12096
	v_mul_f32_e32 v16, v93, v13
	v_mul_f32_e32 v17, v93, v14
	v_cvt_pk_bf16_f32 v16, v16, v16
	v_cvt_pk_bf16_f32 v17, v17, v17
	ds_write_b16 v15, v16 offset:3024
	ds_write_b16 v15, v17 offset:12240
	v_mul_f32_e32 v16, v94, v13
	v_mul_f32_e32 v17, v94, v14
	v_cvt_pk_bf16_f32 v16, v16, v16
	v_cvt_pk_bf16_f32 v17, v17, v17
	ds_write_b16 v15, v16 offset:3168
	ds_write_b16 v15, v17 offset:12384
	v_mul_f32_e32 v16, v95, v13
	v_mul_f32_e32 v17, v95, v14
	v_cvt_pk_bf16_f32 v16, v16, v16
	v_cvt_pk_bf16_f32 v17, v17, v17
	ds_write_b16 v15, v16 offset:3312
	ds_write_b16 v15, v17 offset:12528
	v_mul_f32_e32 v16, v96, v13
	v_mul_f32_e32 v17, v96, v14
	v_cvt_pk_bf16_f32 v16, v16, v16
	v_cvt_pk_bf16_f32 v17, v17, v17
	ds_write_b16 v15, v16 offset:3456
	ds_write_b16 v15, v17 offset:12672
	v_mul_f32_e32 v16, v97, v13
	v_mul_f32_e32 v17, v97, v14
	v_cvt_pk_bf16_f32 v16, v16, v16
	v_cvt_pk_bf16_f32 v17, v17, v17
	ds_write_b16 v15, v16 offset:3600
	ds_write_b16 v15, v17 offset:12816
	v_mul_f32_e32 v16, v98, v13
	v_mul_f32_e32 v17, v98, v14
	v_cvt_pk_bf16_f32 v16, v16, v16
	v_cvt_pk_bf16_f32 v17, v17, v17
	ds_write_b16 v15, v16 offset:3744
	ds_write_b16 v15, v17 offset:12960
	v_mul_f32_e32 v16, v99, v13
	v_mul_f32_e32 v17, v99, v14
	v_cvt_pk_bf16_f32 v16, v16, v16
	v_cvt_pk_bf16_f32 v17, v17, v17
	ds_write_b16 v15, v16 offset:3888
	ds_write_b16 v15, v17 offset:13104
	v_mul_f32_e32 v16, v100, v13
	v_mul_f32_e32 v17, v100, v14
	v_cvt_pk_bf16_f32 v16, v16, v16
	v_cvt_pk_bf16_f32 v17, v17, v17
	ds_write_b16 v15, v16 offset:4032
	ds_write_b16 v15, v17 offset:13248
	v_mul_f32_e32 v16, v101, v13
	v_mul_f32_e32 v17, v101, v14
	v_cvt_pk_bf16_f32 v16, v16, v16
	v_cvt_pk_bf16_f32 v17, v17, v17
	ds_write_b16 v15, v16 offset:4176
	ds_write_b16 v15, v17 offset:13392
	v_mul_f32_e32 v16, v102, v13
	v_mul_f32_e32 v17, v102, v14
	v_cvt_pk_bf16_f32 v16, v16, v16
	v_cvt_pk_bf16_f32 v17, v17, v17
	ds_write_b16 v15, v16 offset:4320
	ds_write_b16 v15, v17 offset:13536
	v_mul_f32_e32 v16, v103, v13
	v_mul_f32_e32 v17, v103, v14
	v_cvt_pk_bf16_f32 v16, v16, v16
	v_cvt_pk_bf16_f32 v17, v17, v17
	ds_write_b16 v15, v16 offset:4464
	ds_write_b16 v15, v17 offset:13680
	v_lshrrev_b32_e32 v18, 3, v21
	v_and_b32_e32 v19, 7, v21
	v_mul_u32_u24_e32 v18, 0x90, v18
	s_mul_i32 s24, s10, 0x4800
	v_lshl_add_u32 v18, v19, 3, v18
	v_mov_b32_e32 v16, 0
	v_add3_u32 v18, v61, v18, s24
	v_mov_b32_e32 v17, 0
	ds_write_b64 v18, v[16:17] offset:64
	ds_write_b64 v18, v[16:17] offset:9280
	ds_write_b64 v18, v[16:17] offset:1216
	ds_write_b64 v18, v[16:17] offset:10432
	ds_write_b64 v18, v[16:17] offset:2368
	ds_write_b64 v18, v[16:17] offset:11584
	ds_write_b64 v18, v[16:17] offset:3520
	ds_write_b64 v18, v[16:17] offset:12736
